# v33 + attention phase: static s_setprio 1 for waves 0-3 (timing-only)
# speedup vs baseline: 1.0038x; 1.0038x over previous
.LBB0_845:
	s_cmp_lt_i32 s92, 9
	s_cselect_b64 s[2:3], -1, 0
	s_and_b64 s[0:1], s[2:3], s[0:1]
	v_writelane_b32 v254, s0, 6
	s_andn2_b64 vcc, exec, s[0:1]
	s_nop 0
	v_writelane_b32 v254, s1, 7
	v_writelane_b32 v254, s85, 8
	v_writelane_b32 v254, s76, 9
	s_nop 1
	v_writelane_b32 v254, s77, 10
	s_cbranch_vccnz .LBB0_1552
	s_cmp_ge_u32 s89, 4
	s_cbranch_scc1 .Lp8_prio_done
	s_setprio 1
